# shared conversion loop: next queue claim issued before the item's last 16 stores; loop top uses the prefetched index with a counted vmcnt(16) (no store drain, no atomic round trip per item)
# baseline (speedup 1.0000x reference)
.LBB0_1288:
	v_mul_u32_u24_e32 v2, s28, v134
	v_mul_u32_u24_e32 v4, s28, v135
	v_mul_u32_u24_e32 v6, s28, v136
	v_mul_u32_u24_e32 v8, s28, v137
	v_mul_u32_u24_e32 v10, s28, v138
	v_mul_u32_u24_e32 v12, s28, v139
	v_mul_u32_u24_e32 v16, s28, v140
	v_mul_u32_u24_e32 v30, s28, v141
	v_lshl_add_u64 v[14:15], s[26:27], 0, v[130:131]
	v_lshlrev_b32_e32 v2, 2, v2
	v_mov_b32_e32 v3, v131
	v_lshlrev_b32_e32 v4, 2, v4
	v_mov_b32_e32 v5, v131
	v_lshlrev_b32_e32 v6, 2, v6
	v_mov_b32_e32 v7, v131
	v_lshlrev_b32_e32 v8, 2, v8
	v_mov_b32_e32 v9, v131
	v_lshlrev_b32_e32 v10, 2, v10
	v_mov_b32_e32 v11, v131
	v_lshlrev_b32_e32 v12, 2, v12
	v_mov_b32_e32 v13, v131
	v_lshlrev_b32_e32 v16, 2, v16
	v_mov_b32_e32 v17, v131
	v_lshlrev_b32_e32 v30, 2, v30
	v_mov_b32_e32 v31, v131
	v_lshl_add_u64 v[2:3], v[14:15], 0, v[2:3]
	v_lshl_add_u64 v[4:5], v[14:15], 0, v[4:5]
	v_lshl_add_u64 v[6:7], v[14:15], 0, v[6:7]
	v_lshl_add_u64 v[8:9], v[14:15], 0, v[8:9]
	v_lshl_add_u64 v[10:11], v[14:15], 0, v[10:11]
	v_lshl_add_u64 v[12:13], v[14:15], 0, v[12:13]
	v_lshl_add_u64 v[16:17], v[14:15], 0, v[16:17]
	v_lshl_add_u64 v[14:15], v[14:15], 0, v[30:31]
	s_waitcnt vmcnt(34)
	v_pk_mul_f32 v[34:35], v[34:35], s[2:3] op_sel_hi:[1,0]
	global_load_dwordx4 v[18:21], v[2:3], off nt
	s_nop 0
	global_load_dwordx4 v[2:5], v[4:5], off nt
	s_nop 0
	global_load_dwordx4 v[22:25], v[6:7], off nt
	s_nop 0
	global_load_dwordx4 v[6:9], v[8:9], off nt
	s_nop 0
	global_load_dwordx4 v[26:29], v[10:11], off nt
	s_nop 0
	global_load_dwordx4 v[10:13], v[12:13], off nt
	s_nop 0
	global_load_dwordx4 v[30:33], v[16:17], off nt
	s_nop 0
	global_load_dwordx4 v[14:17], v[14:15], off nt
	s_mov_b64 s[40:41], exec
	v_readlane_b32 s42, v254, 5
	v_readlane_b32 s43, v254, 6
	s_and_b64 s[42:43], s[40:41], s[42:43]
	s_mov_b64 exec, s[42:43]
	s_cbranch_execz mkcq_nolate
	v_mov_b32_e32 v200, 1
	v_mov_b32_e32 v201, s101
	global_atomic_add v200, v201, v200, s[96:97] offset:768 sc0
mkcq_nolate:
	s_mov_b64 exec, s[40:41]
	s_bitset1_b32 s98, 4
	ds_write2_b32 v145, v34, v35 offset1:1
	v_pk_mul_f32 v[34:35], v[36:37], s[2:3] op_sel_hi:[1,0]
	ds_write2_b32 v146, v34, v35 offset1:1
	s_waitcnt vmcnt(41)
	v_pk_mul_f32 v[34:35], v[54:55], s[2:3] op_sel_hi:[1,0]
	ds_write2_b32 v147, v34, v35 offset1:1
	v_pk_mul_f32 v[34:35], v[56:57], s[2:3] op_sel_hi:[1,0]
	ds_write2_b32 v148, v34, v35 offset1:1
	s_waitcnt vmcnt(40)
	v_pk_mul_f32 v[34:35], v[38:39], s[2:3] op_sel_hi:[1,0]
	ds_write2_b32 v149, v34, v35 offset1:1
	v_pk_mul_f32 v[34:35], v[40:41], s[2:3] op_sel_hi:[1,0]
	ds_write2_b32 v150, v34, v35 offset1:1
	s_waitcnt vmcnt(39)
	v_pk_mul_f32 v[34:35], v[58:59], s[2:3] op_sel_hi:[1,0]
	ds_write2_b32 v151, v34, v35 offset1:1
	v_pk_mul_f32 v[34:35], v[60:61], s[2:3] op_sel_hi:[1,0]
	ds_write2_b32 v152, v34, v35 offset1:1
	s_waitcnt vmcnt(38)
	v_pk_mul_f32 v[34:35], v[42:43], s[2:3] op_sel_hi:[1,0]
	ds_write2_b32 v153, v34, v35 offset1:1
	v_pk_mul_f32 v[34:35], v[44:45], s[2:3] op_sel_hi:[1,0]
	ds_write2_b32 v154, v34, v35 offset1:1
	s_waitcnt vmcnt(37)
	v_pk_mul_f32 v[34:35], v[62:63], s[2:3] op_sel_hi:[1,0]
	ds_write2_b32 v155, v34, v35 offset1:1
	v_pk_mul_f32 v[34:35], v[64:65], s[2:3] op_sel_hi:[1,0]
	v_pk_mul_f32 v[50:51], v[50:51], s[2:3] op_sel_hi:[1,0]
	ds_write2_b32 v156, v34, v35 offset1:1
	s_waitcnt vmcnt(36)
	v_pk_mul_f32 v[34:35], v[46:47], s[2:3] op_sel_hi:[1,0]
	ds_write2_b32 v144, v50, v51 offset1:1
	v_pk_mul_f32 v[50:51], v[52:53], s[2:3] op_sel_hi:[1,0]
	ds_write2_b32 v157, v34, v35 offset1:1
	v_pk_mul_f32 v[34:35], v[48:49], s[2:3] op_sel_hi:[1,0]
	ds_write2_b32 v144, v50, v51 offset0:2 offset1:3
	ds_write2_b32 v158, v34, v35 offset1:1
	s_waitcnt lgkmcnt(0)
	ds_read2_b32 v[34:35], v142 offset0:33 offset1:41
	ds_read2_b32 v[36:37], v142 offset0:66 offset1:74
	ds_read2_b32 v[38:39], v142 offset1:8
	ds_read2_b32 v[40:41], v142 offset0:99 offset1:107
	ds_read2_b32 v[44:45], v142 offset0:132 offset1:140
	ds_read2_b32 v[46:47], v142 offset0:165 offset1:173
	v_mov_b32_e32 v42, v131
	ds_read2_b32 v[48:49], v142 offset0:198 offset1:206
	ds_read2_b32 v[50:51], v142 offset0:231 offset1:239
	v_mov_b32_e32 v43, v131
	s_waitcnt lgkmcnt(5)
	v_cvt_pk_fp8_f32 v42, v38, v34
	s_waitcnt lgkmcnt(2)
	v_cvt_pk_fp8_f32 v43, v44, v46
	v_mov_b32_e32 v34, v131
	v_cvt_pk_fp8_f32 v34, v39, v35
	v_cvt_pk_fp8_f32 v42, v36, v40 op_sel:[0,0,1]
	s_waitcnt lgkmcnt(0)
	v_cvt_pk_fp8_f32 v43, v48, v50 op_sel:[0,0,1]
	v_mov_b32_e32 v35, v131
	v_cvt_pk_fp8_f32 v35, v45, v47
	v_lshl_add_u64 v[52:53], s[10:11], 0, v[132:133]
	v_mad_u64_u32 v[38:39], s[10:11], s6, v134, v[52:53]
	global_store_dwordx2 v[38:39], v[42:43], off nt
	v_cvt_pk_fp8_f32 v34, v37, v41 op_sel:[0,0,1]
	v_cvt_pk_fp8_f32 v35, v49, v51 op_sel:[0,0,1]
	ds_read2_b32 v[36:37], v142 offset0:16 offset1:24
	ds_read2_b32 v[38:39], v142 offset0:49 offset1:57
	ds_read2_b32 v[40:41], v142 offset0:82 offset1:90
	ds_read2_b32 v[42:43], v142 offset0:115 offset1:123
	ds_read2_b32 v[46:47], v142 offset0:148 offset1:156
	ds_read2_b32 v[48:49], v142 offset0:181 offset1:189
	v_mov_b32_e32 v44, v131
	ds_read2_b32 v[50:51], v142 offset0:214 offset1:222
	ds_read2_b32 v[54:55], v142 offset0:247 offset1:255
	v_mov_b32_e32 v45, v131
	v_mad_u64_u32 v[56:57], s[10:11], s6, v135, v[52:53]
	s_waitcnt lgkmcnt(6)
	v_cvt_pk_fp8_f32 v44, v36, v38
	s_waitcnt lgkmcnt(2)
	v_cvt_pk_fp8_f32 v45, v46, v48
	global_store_dwordx2 v[56:57], v[34:35], off nt
	v_mov_b32_e32 v34, v131
	v_mov_b32_e32 v35, v131
	v_cvt_pk_fp8_f32 v34, v37, v39
	v_cvt_pk_fp8_f32 v35, v47, v49
	v_cvt_pk_fp8_f32 v44, v40, v42 op_sel:[0,0,1]
	s_waitcnt lgkmcnt(0)
	v_cvt_pk_fp8_f32 v45, v50, v54 op_sel:[0,0,1]
	v_cvt_pk_fp8_f32 v34, v41, v43 op_sel:[0,0,1]
	v_cvt_pk_fp8_f32 v35, v51, v55 op_sel:[0,0,1]
	v_mad_u64_u32 v[36:37], s[10:11], s6, v136, v[52:53]
	global_store_dwordx2 v[36:37], v[44:45], off nt
	v_mad_u64_u32 v[36:37], s[6:7], s6, v137, v[52:53]
	global_store_dwordx2 v[36:37], v[34:35], off nt
	s_waitcnt lgkmcnt(0)
	s_waitcnt vmcnt(35)
	v_pk_mul_f32 v[34:35], v[114:115], s[2:3] op_sel_hi:[1,0]
	ds_write2_b32 v144, v34, v35 offset1:1
	v_pk_mul_f32 v[34:35], v[116:117], s[2:3] op_sel_hi:[1,0]
	ds_write2_b32 v144, v34, v35 offset0:2 offset1:3
	s_waitcnt vmcnt(34)
	v_pk_mul_f32 v[34:35], v[98:99], s[2:3] op_sel_hi:[1,0]
	ds_write2_b32 v145, v34, v35 offset1:1
	v_pk_mul_f32 v[34:35], v[100:101], s[2:3] op_sel_hi:[1,0]
	ds_write2_b32 v146, v34, v35 offset1:1
	s_waitcnt vmcnt(33)
	v_pk_mul_f32 v[34:35], v[118:119], s[2:3] op_sel_hi:[1,0]
	ds_write2_b32 v147, v34, v35 offset1:1
	v_pk_mul_f32 v[34:35], v[120:121], s[2:3] op_sel_hi:[1,0]
	ds_write2_b32 v148, v34, v35 offset1:1
	s_waitcnt vmcnt(32)
	v_pk_mul_f32 v[34:35], v[102:103], s[2:3] op_sel_hi:[1,0]
	ds_write2_b32 v149, v34, v35 offset1:1
	v_pk_mul_f32 v[34:35], v[104:105], s[2:3] op_sel_hi:[1,0]
	ds_write2_b32 v150, v34, v35 offset1:1
	s_waitcnt vmcnt(31)
	v_pk_mul_f32 v[34:35], v[122:123], s[2:3] op_sel_hi:[1,0]
	ds_write2_b32 v151, v34, v35 offset1:1
	v_pk_mul_f32 v[34:35], v[124:125], s[2:3] op_sel_hi:[1,0]
	ds_write2_b32 v152, v34, v35 offset1:1
	s_waitcnt vmcnt(30)
	v_pk_mul_f32 v[34:35], v[106:107], s[2:3] op_sel_hi:[1,0]
	ds_write2_b32 v153, v34, v35 offset1:1
	v_pk_mul_f32 v[34:35], v[108:109], s[2:3] op_sel_hi:[1,0]
	ds_write2_b32 v154, v34, v35 offset1:1
	s_waitcnt vmcnt(29)
	v_pk_mul_f32 v[34:35], v[126:127], s[2:3] op_sel_hi:[1,0]
	ds_write2_b32 v155, v34, v35 offset1:1
	v_pk_mul_f32 v[34:35], v[128:129], s[2:3] op_sel_hi:[1,0]
	ds_write2_b32 v156, v34, v35 offset1:1
	s_waitcnt vmcnt(28)
	v_pk_mul_f32 v[34:35], v[110:111], s[2:3] op_sel_hi:[1,0]
	ds_write2_b32 v157, v34, v35 offset1:1
	v_pk_mul_f32 v[34:35], v[112:113], s[2:3] op_sel_hi:[1,0]
	ds_write2_b32 v158, v34, v35 offset1:1
	s_waitcnt lgkmcnt(0)
	ds_read2_b32 v[34:35], v142 offset0:33 offset1:41
	ds_read2_b32 v[36:37], v142 offset0:66 offset1:74
	ds_read2_b32 v[38:39], v142 offset1:8
	ds_read2_b32 v[40:41], v142 offset0:99 offset1:107
	ds_read2_b32 v[44:45], v142 offset0:132 offset1:140
	ds_read2_b32 v[46:47], v142 offset0:165 offset1:173
	v_mov_b32_e32 v42, v131
	ds_read2_b32 v[48:49], v142 offset0:198 offset1:206
	ds_read2_b32 v[50:51], v142 offset0:231 offset1:239
	v_mov_b32_e32 v43, v131
	s_waitcnt lgkmcnt(5)
	v_cvt_pk_fp8_f32 v42, v38, v34
	s_waitcnt lgkmcnt(2)
	v_cvt_pk_fp8_f32 v43, v44, v46
	v_mov_b32_e32 v34, v131
	v_cvt_pk_fp8_f32 v34, v39, v35
	v_cvt_pk_fp8_f32 v42, v36, v40 op_sel:[0,0,1]
	s_waitcnt lgkmcnt(0)
	v_cvt_pk_fp8_f32 v43, v48, v50 op_sel:[0,0,1]
	v_mov_b32_e32 v35, v131
	v_cvt_pk_fp8_f32 v35, v45, v47
	v_lshl_add_u64 v[52:53], s[24:25], 0, v[132:133]
	v_mad_u64_u32 v[38:39], s[6:7], s22, v134, v[52:53]
	global_store_dwordx2 v[38:39], v[42:43], off nt
	v_cvt_pk_fp8_f32 v34, v37, v41 op_sel:[0,0,1]
	v_cvt_pk_fp8_f32 v35, v49, v51 op_sel:[0,0,1]
	ds_read2_b32 v[36:37], v142 offset0:16 offset1:24
	ds_read2_b32 v[38:39], v142 offset0:49 offset1:57
	ds_read2_b32 v[40:41], v142 offset0:82 offset1:90
	ds_read2_b32 v[42:43], v142 offset0:115 offset1:123
	ds_read2_b32 v[46:47], v142 offset0:148 offset1:156
	ds_read2_b32 v[48:49], v142 offset0:181 offset1:189
	v_mov_b32_e32 v44, v131
	ds_read2_b32 v[50:51], v142 offset0:214 offset1:222
	ds_read2_b32 v[54:55], v142 offset0:247 offset1:255
	v_mov_b32_e32 v45, v131
	v_mad_u64_u32 v[56:57], s[6:7], s22, v135, v[52:53]
	s_waitcnt lgkmcnt(6)
	v_cvt_pk_fp8_f32 v44, v36, v38
	s_waitcnt lgkmcnt(2)
	v_cvt_pk_fp8_f32 v45, v46, v48
	global_store_dwordx2 v[56:57], v[34:35], off nt
	v_mov_b32_e32 v34, v131
	v_mov_b32_e32 v35, v131
	v_cvt_pk_fp8_f32 v34, v37, v39
	v_cvt_pk_fp8_f32 v35, v47, v49
	v_cvt_pk_fp8_f32 v44, v40, v42 op_sel:[0,0,1]
	s_waitcnt lgkmcnt(0)
	v_cvt_pk_fp8_f32 v45, v50, v54 op_sel:[0,0,1]
	v_cvt_pk_fp8_f32 v34, v41, v43 op_sel:[0,0,1]
	v_cvt_pk_fp8_f32 v35, v51, v55 op_sel:[0,0,1]
	v_mad_u64_u32 v[36:37], s[6:7], s22, v136, v[52:53]
	global_store_dwordx2 v[36:37], v[44:45], off nt
	v_mad_u64_u32 v[36:37], s[6:7], s22, v137, v[52:53]
	global_store_dwordx2 v[36:37], v[34:35], off nt
	s_waitcnt lgkmcnt(0)
	s_waitcnt vmcnt(27)
	v_pk_mul_f32 v[34:35], v[82:83], s[2:3] op_sel_hi:[1,0]
	ds_write2_b32 v144, v34, v35 offset1:1
	v_pk_mul_f32 v[34:35], v[84:85], s[2:3] op_sel_hi:[1,0]
	ds_write2_b32 v144, v34, v35 offset0:2 offset1:3
	s_waitcnt vmcnt(26)
	v_pk_mul_f32 v[34:35], v[66:67], s[2:3] op_sel_hi:[1,0]
	ds_write2_b32 v145, v34, v35 offset1:1
	v_pk_mul_f32 v[34:35], v[68:69], s[2:3] op_sel_hi:[1,0]
	ds_write2_b32 v146, v34, v35 offset1:1
	s_waitcnt vmcnt(25)
	v_pk_mul_f32 v[34:35], v[86:87], s[2:3] op_sel_hi:[1,0]
	ds_write2_b32 v147, v34, v35 offset1:1
	v_pk_mul_f32 v[34:35], v[88:89], s[2:3] op_sel_hi:[1,0]
	ds_write2_b32 v148, v34, v35 offset1:1
	s_waitcnt vmcnt(24)
	v_pk_mul_f32 v[34:35], v[70:71], s[2:3] op_sel_hi:[1,0]
	ds_write2_b32 v149, v34, v35 offset1:1
	v_pk_mul_f32 v[34:35], v[72:73], s[2:3] op_sel_hi:[1,0]
	ds_write2_b32 v150, v34, v35 offset1:1
	s_waitcnt vmcnt(23)
	v_pk_mul_f32 v[34:35], v[90:91], s[2:3] op_sel_hi:[1,0]
	ds_write2_b32 v151, v34, v35 offset1:1
	v_pk_mul_f32 v[34:35], v[92:93], s[2:3] op_sel_hi:[1,0]
	ds_write2_b32 v152, v34, v35 offset1:1
	s_waitcnt vmcnt(22)
	v_pk_mul_f32 v[34:35], v[74:75], s[2:3] op_sel_hi:[1,0]
	ds_write2_b32 v153, v34, v35 offset1:1
	v_pk_mul_f32 v[34:35], v[76:77], s[2:3] op_sel_hi:[1,0]
	ds_write2_b32 v154, v34, v35 offset1:1
	s_waitcnt vmcnt(21)
	v_pk_mul_f32 v[34:35], v[94:95], s[2:3] op_sel_hi:[1,0]
	ds_write2_b32 v155, v34, v35 offset1:1
	v_pk_mul_f32 v[34:35], v[96:97], s[2:3] op_sel_hi:[1,0]
	ds_write2_b32 v156, v34, v35 offset1:1
	s_waitcnt vmcnt(20)
	v_pk_mul_f32 v[34:35], v[78:79], s[2:3] op_sel_hi:[1,0]
	ds_write2_b32 v157, v34, v35 offset1:1
	v_pk_mul_f32 v[34:35], v[80:81], s[2:3] op_sel_hi:[1,0]
	ds_write2_b32 v158, v34, v35 offset1:1
	s_waitcnt lgkmcnt(0)
	ds_read2_b32 v[34:35], v142 offset0:33 offset1:41
	ds_read2_b32 v[36:37], v142 offset0:66 offset1:74
	ds_read2_b32 v[38:39], v142 offset1:8
	ds_read2_b32 v[40:41], v142 offset0:99 offset1:107
	ds_read2_b32 v[44:45], v142 offset0:132 offset1:140
	ds_read2_b32 v[46:47], v142 offset0:165 offset1:173
	v_mov_b32_e32 v42, v131
	ds_read2_b32 v[48:49], v142 offset0:198 offset1:206
	ds_read2_b32 v[50:51], v142 offset0:231 offset1:239
	v_mov_b32_e32 v43, v131
	s_waitcnt lgkmcnt(5)
	v_cvt_pk_fp8_f32 v42, v38, v34
	s_waitcnt lgkmcnt(2)
	v_cvt_pk_fp8_f32 v43, v44, v46
	v_mov_b32_e32 v34, v131
	v_cvt_pk_fp8_f32 v34, v39, v35
	v_cvt_pk_fp8_f32 v42, v36, v40 op_sel:[0,0,1]
	s_waitcnt lgkmcnt(0)
	v_cvt_pk_fp8_f32 v43, v48, v50 op_sel:[0,0,1]
	v_mov_b32_e32 v35, v131
	v_cvt_pk_fp8_f32 v35, v45, v47
	v_lshl_add_u64 v[52:53], s[20:21], 0, v[132:133]
	v_mad_u64_u32 v[38:39], s[6:7], s18, v134, v[52:53]
	global_store_dwordx2 v[38:39], v[42:43], off nt
	v_cvt_pk_fp8_f32 v34, v37, v41 op_sel:[0,0,1]
	v_cvt_pk_fp8_f32 v35, v49, v51 op_sel:[0,0,1]
	ds_read2_b32 v[36:37], v142 offset0:16 offset1:24
	ds_read2_b32 v[38:39], v142 offset0:49 offset1:57
	ds_read2_b32 v[40:41], v142 offset0:82 offset1:90
	ds_read2_b32 v[42:43], v142 offset0:115 offset1:123
	ds_read2_b32 v[46:47], v142 offset0:148 offset1:156
	ds_read2_b32 v[48:49], v142 offset0:181 offset1:189
	v_mov_b32_e32 v44, v131
	ds_read2_b32 v[50:51], v142 offset0:214 offset1:222
	ds_read2_b32 v[54:55], v142 offset0:247 offset1:255
	v_mov_b32_e32 v45, v131
	v_mad_u64_u32 v[56:57], s[6:7], s18, v135, v[52:53]
	s_waitcnt lgkmcnt(6)
	v_cvt_pk_fp8_f32 v44, v36, v38
	s_waitcnt lgkmcnt(2)
	v_cvt_pk_fp8_f32 v45, v46, v48
	global_store_dwordx2 v[56:57], v[34:35], off nt
	v_mov_b32_e32 v34, v131
	v_mov_b32_e32 v35, v131
	v_cvt_pk_fp8_f32 v34, v37, v39
	v_cvt_pk_fp8_f32 v35, v47, v49
	v_cvt_pk_fp8_f32 v44, v40, v42 op_sel:[0,0,1]
	s_waitcnt lgkmcnt(0)
	v_cvt_pk_fp8_f32 v45, v50, v54 op_sel:[0,0,1]
	v_cvt_pk_fp8_f32 v34, v41, v43 op_sel:[0,0,1]
	v_cvt_pk_fp8_f32 v35, v51, v55 op_sel:[0,0,1]
	v_mad_u64_u32 v[36:37], s[6:7], s18, v136, v[52:53]
	global_store_dwordx2 v[36:37], v[44:45], off nt
	v_mad_u64_u32 v[36:37], s[6:7], s18, v137, v[52:53]
	global_store_dwordx2 v[36:37], v[34:35], off nt
	s_waitcnt lgkmcnt(0)
	s_waitcnt vmcnt(18)
	v_pk_mul_f32 v[2:3], v[2:3], s[2:3] op_sel_hi:[1,0]
	ds_write2_b32 v145, v2, v3 offset1:1
	v_pk_mul_f32 v[2:3], v[4:5], s[2:3] op_sel_hi:[1,0]
	ds_write2_b32 v146, v2, v3 offset1:1
	s_waitcnt vmcnt(17)
	v_pk_mul_f32 v[2:3], v[22:23], s[2:3] op_sel_hi:[1,0]
	ds_write2_b32 v147, v2, v3 offset1:1
	v_pk_mul_f32 v[2:3], v[24:25], s[2:3] op_sel_hi:[1,0]
	ds_write2_b32 v148, v2, v3 offset1:1
	s_waitcnt vmcnt(16)
	v_pk_mul_f32 v[2:3], v[6:7], s[2:3] op_sel_hi:[1,0]
	ds_write2_b32 v149, v2, v3 offset1:1
	v_pk_mul_f32 v[2:3], v[8:9], s[2:3] op_sel_hi:[1,0]
	ds_write2_b32 v150, v2, v3 offset1:1
	s_waitcnt vmcnt(15)
	v_pk_mul_f32 v[2:3], v[26:27], s[2:3] op_sel_hi:[1,0]
	ds_write2_b32 v151, v2, v3 offset1:1
	v_pk_mul_f32 v[2:3], v[28:29], s[2:3] op_sel_hi:[1,0]
	ds_write2_b32 v152, v2, v3 offset1:1
	s_waitcnt vmcnt(14)
	v_pk_mul_f32 v[2:3], v[10:11], s[2:3] op_sel_hi:[1,0]
	ds_write2_b32 v153, v2, v3 offset1:1
	v_pk_mul_f32 v[2:3], v[12:13], s[2:3] op_sel_hi:[1,0]
	ds_write2_b32 v154, v2, v3 offset1:1
	s_waitcnt vmcnt(13)
	v_pk_mul_f32 v[2:3], v[30:31], s[2:3] op_sel_hi:[1,0]
	ds_write2_b32 v155, v2, v3 offset1:1
	v_pk_mul_f32 v[2:3], v[32:33], s[2:3] op_sel_hi:[1,0]
	v_pk_mul_f32 v[18:19], v[18:19], s[2:3] op_sel_hi:[1,0]
	ds_write2_b32 v156, v2, v3 offset1:1
	s_waitcnt vmcnt(12)
	v_pk_mul_f32 v[2:3], v[14:15], s[2:3] op_sel_hi:[1,0]
	ds_write2_b32 v144, v18, v19 offset1:1
	v_pk_mul_f32 v[18:19], v[20:21], s[2:3] op_sel_hi:[1,0]
	ds_write2_b32 v157, v2, v3 offset1:1
	v_pk_mul_f32 v[2:3], v[16:17], s[2:3] op_sel_hi:[1,0]
	ds_write2_b32 v144, v18, v19 offset0:2 offset1:3
	ds_write2_b32 v158, v2, v3 offset1:1
	s_waitcnt lgkmcnt(0)
	ds_read2_b32 v[2:3], v142 offset0:33 offset1:41
	ds_read2_b32 v[4:5], v142 offset0:66 offset1:74
	ds_read2_b32 v[6:7], v142 offset1:8
	ds_read2_b32 v[8:9], v142 offset0:99 offset1:107
	ds_read2_b32 v[12:13], v142 offset0:132 offset1:140
	ds_read2_b32 v[14:15], v142 offset0:165 offset1:173
	v_mov_b32_e32 v10, v131
	ds_read2_b32 v[16:17], v142 offset0:198 offset1:206
	ds_read2_b32 v[18:19], v142 offset0:231 offset1:239
	v_mov_b32_e32 v11, v131
	s_waitcnt lgkmcnt(5)
	v_cvt_pk_fp8_f32 v10, v6, v2
	s_waitcnt lgkmcnt(2)
	v_cvt_pk_fp8_f32 v11, v12, v14
	v_mov_b32_e32 v2, v131
	v_cvt_pk_fp8_f32 v2, v7, v3
	v_cvt_pk_fp8_f32 v10, v4, v8 op_sel:[0,0,1]
	s_waitcnt lgkmcnt(0)
	v_cvt_pk_fp8_f32 v11, v16, v18 op_sel:[0,0,1]
	v_mov_b32_e32 v3, v131
	v_cvt_pk_fp8_f32 v3, v13, v15
	v_lshl_add_u64 v[20:21], s[8:9], 0, v[132:133]
	v_mad_u64_u32 v[6:7], s[6:7], s4, v134, v[20:21]
	global_store_dwordx2 v[6:7], v[10:11], off nt
	v_cvt_pk_fp8_f32 v2, v5, v9 op_sel:[0,0,1]
	v_cvt_pk_fp8_f32 v3, v17, v19 op_sel:[0,0,1]
	ds_read2_b32 v[4:5], v142 offset0:16 offset1:24
	ds_read2_b32 v[6:7], v142 offset0:49 offset1:57
	ds_read2_b32 v[8:9], v142 offset0:82 offset1:90
	ds_read2_b32 v[10:11], v142 offset0:115 offset1:123
	ds_read2_b32 v[14:15], v142 offset0:148 offset1:156
	ds_read2_b32 v[16:17], v142 offset0:181 offset1:189
	v_mov_b32_e32 v12, v131
	ds_read2_b32 v[18:19], v142 offset0:214 offset1:222
	ds_read2_b32 v[22:23], v142 offset0:247 offset1:255
	v_mov_b32_e32 v13, v131
	v_mad_u64_u32 v[24:25], s[6:7], s4, v135, v[20:21]
	s_waitcnt lgkmcnt(6)
	v_cvt_pk_fp8_f32 v12, v4, v6
	s_waitcnt lgkmcnt(2)
	v_cvt_pk_fp8_f32 v13, v14, v16
	global_store_dwordx2 v[24:25], v[2:3], off nt
	v_mov_b32_e32 v2, v131
	v_mov_b32_e32 v3, v131
	v_cvt_pk_fp8_f32 v2, v5, v7
	v_cvt_pk_fp8_f32 v3, v15, v17
	v_cvt_pk_fp8_f32 v12, v8, v10 op_sel:[0,0,1]
	s_waitcnt lgkmcnt(0)
	v_cvt_pk_fp8_f32 v13, v18, v22 op_sel:[0,0,1]
	v_cvt_pk_fp8_f32 v2, v9, v11 op_sel:[0,0,1]
	v_cvt_pk_fp8_f32 v3, v19, v23 op_sel:[0,0,1]
	v_mad_u64_u32 v[4:5], s[6:7], s4, v136, v[20:21]
	global_store_dwordx2 v[4:5], v[12:13], off nt
	v_mad_u64_u32 v[4:5], s[4:5], s4, v137, v[20:21]
	global_store_dwordx2 v[4:5], v[2:3], off nt
	s_waitcnt lgkmcnt(0)
	s_mov_b64 s[4:5], 0

.LBB0_1290:
	s_barrier
	s_mov_b64 s[4:5], exec
	v_readlane_b32 s6, v254, 5
	v_readlane_b32 s7, v254, 6
	s_and_b64 s[6:7], s[4:5], s[6:7]
	s_mov_b64 exec, s[6:7]
	s_cbranch_execz .LBB0_1294
	s_mov_b64 s[8:9], exec
	v_mbcnt_lo_u32_b32 v2, s8, 0
	v_mbcnt_hi_u32_b32 v2, s9, v2
	v_cmp_eq_u32_e32 vcc, 0, v2
	s_and_saveexec_b64 s[6:7], vcc
	s_cbranch_execz .LBB0_1293
	s_bitcmp1_b32 s98, 4
	s_cbranch_scc1 mkcq_pf
	s_bcnt1_i32_b64 s0, s[8:9]
	v_mov_b32_e32 v3, s0
	v_mov_b32_e32 v6, s101
	global_atomic_add v3, v6, v3, s[96:97] offset:768 sc0
	s_waitcnt vmcnt(0)
	s_branch .LBB0_1293
mkcq_pf:
	s_waitcnt vmcnt(16)
	v_mov_b32_e32 v3, v200
.LBB0_1293:
	s_or_b64 exec, exec, s[6:7]
	v_readfirstlane_b32 s0, v3
	v_mov_b32_e32 v3, s33
	s_nop 0
	v_add_u32_e32 v2, s0, v2
	v_add_u32_e32 v2, s99, v2
	ds_write_b32 v3, v2

.LBB0_1334:
	s_bitset0_b32 s98, 4
	s_cmp_eq_u32 s98, 1
	s_cbranch_scc1 mkcq_p3ret
	v_readlane_b32 s48, v254, 53
	v_readlane_b32 s49, v254, 54
	s_cmp_lt_i32 s49, 9
	s_barrier
	s_cbranch_scc1 .LBB0_1388
	s_waitcnt vmcnt(0)
	s_barrier
	s_mov_b64 s[0:1], exec
	v_readlane_b32 s2, v254, 5
	v_readlane_b32 s3, v254, 6
	s_and_b64 s[2:3], s[0:1], s[2:3]
	s_mov_b64 exec, s[2:3]
	s_cbranch_execz .LBB0_1387
	s_add_i32 s2, 0, 0x26160
	v_mov_b32_e32 v2, s2
	s_waitcnt vmcnt(0) expcnt(0) lgkmcnt(0)
	ds_read_b32 v4, v2
	s_add_i32 s2, 0, 0x26164
	v_mov_b32_e32 v2, s2
	ds_read_b32 v2, v2
	s_waitcnt lgkmcnt(1)
	v_cmp_ne_u32_e32 vcc, 0, v4
	s_cbranch_vccnz .LBB0_1351
	v_readlane_b32 s2, v254, 0
	v_readlane_b32 s3, v254, 1
	s_load_dwordx2 s[6:7], s[2:3], 0x4
	s_add_u32 s2, s96, 0x4200
	s_addc_u32 s3, s97, 0
	s_add_u32 s4, s96, 0x4400
	s_addc_u32 s5, s97, 0
	s_waitcnt lgkmcnt(0)
	s_mul_i32 s33, s6, s72
	s_add_u32 s6, s96, 0x4500
	s_mul_i32 s33, s33, s7
	s_addc_u32 s7, s97, 0
	s_add_u32 s8, s96, 0x4600
	s_addc_u32 s9, s97, 0
	s_add_u32 s10, s96, 0x4700
	s_addc_u32 s11, s97, 0
	s_add_u32 s18, s96, 0x4800
	s_addc_u32 s19, s97, 0
	s_add_u32 s20, s96, 0x4900
	s_addc_u32 s21, s97, 0
	s_add_u32 s22, s96, 0x4a00
	s_addc_u32 s23, s97, 0
	s_add_u32 s24, s96, 0x4b00
	s_addc_u32 s25, s97, 0
	s_add_u32 s26, s96, 0x4c00
	s_addc_u32 s27, s97, 0
	s_add_u32 s28, s96, 0x4d00
	s_addc_u32 s29, s97, 0
	s_add_u32 s30, s96, 0x4e00
	s_addc_u32 s31, s97, 0
	s_add_u32 s34, s96, 0x4f00
	s_addc_u32 s35, s97, 0
	s_add_u32 s36, s96, 0x5000
	s_addc_u32 s37, s97, 0
	s_add_u32 s38, s96, 0x5100
	s_addc_u32 s39, s97, 0
	s_add_u32 s40, s96, 0x5200
	s_addc_u32 s41, s97, 0
	s_add_u32 s42, s96, 0x5300
	s_addc_u32 s43, s97, 0
	s_mov_b32 s50, 1
	v_mov_b32_e32 v18, 0
	s_branch .LBB0_1339
